# attention loop: LDS tile writes and next-tile global loads spread one per MFMA gap (gaps 8-14) instead of one burst, running tile counters
# speedup vs baseline: 1.0609x; 1.0086x over previous
.LBB0_1138:
	v_mov_b32_e32 v224, 0
	s_mov_b32 s1, 0
	v_mov_b32_e32 v36, 0
	v_mov_b32_e32 v37, 0
	v_mov_b32_e32 v38, 0
	v_mov_b32_e32 v39, 0
	v_mov_b32_e32 v40, 0
	v_mov_b32_e32 v41, 0
	v_mov_b32_e32 v42, 0
	v_mov_b32_e32 v43, 0
	v_mov_b32_e32 v44, 0
	v_mov_b32_e32 v45, 0
	v_mov_b32_e32 v46, 0
	v_mov_b32_e32 v47, 0
	v_mov_b32_e32 v48, 0
	v_mov_b32_e32 v49, 0
	v_mov_b32_e32 v50, 0
	v_mov_b32_e32 v51, 0
	v_mov_b32_e32 v52, 0
	v_mov_b32_e32 v53, 0
	v_mov_b32_e32 v54, 0
	v_mov_b32_e32 v55, 0
	v_mov_b32_e32 v56, 0
	v_mov_b32_e32 v57, 0
	v_mov_b32_e32 v58, 0
	v_mov_b32_e32 v59, 0
	v_mov_b32_e32 v60, 0
	v_mov_b32_e32 v61, 0
	v_mov_b32_e32 v62, 0
	v_mov_b32_e32 v63, 0
	v_mov_b32_e32 v64, 0
	v_mov_b32_e32 v65, 0
	v_mov_b32_e32 v66, 0
	v_mov_b32_e32 v67, 0
	v_add_u32_e32 v178, v218, v217
	ds_read_b128 v[166:169], v205 offset:13312
	ds_read_b128 v[170:173], v205 offset:19968
	ds_read_b128 v[174:177], v205 offset:13344
	ds_read_b128 v[206:209], v205 offset:20000
	ds_read_b128 v[226:229], v205 offset:13376
	s_add_i32 s2, s23, s1
	s_add_i32 s3, s2, 2
	s_cmp_ge_u32 s2, s34
	s_cselect_b32 s7, s34, 0
	s_sub_i32 s2, s2, s7
	s_cmp_ge_u32 s3, s34
	s_cselect_b32 s7, s34, 0
	s_sub_i32 s3, s3, s7
	s_cmp_ge_u32 s3, s34
	s_cselect_b32 s7, s34, 0
	s_sub_i32 s3, s3, s7
	v_lshl_add_u32 v230, s3, v215, v223
	global_load_dwordx4 v[230:233], v230, s[44:45]
	v_mad_u32_u24 v234, s3, v199, v202
	global_load_dwordx2 v[234:235], v234, s[44:45]
	s_add_i32 s2, s23, s1
	s_add_i32 s3, s2, 3
	s_add_i32 s2, s2, 1
	s_cmp_ge_u32 s2, s34
	s_cselect_b32 s7, s34, 0
	s_sub_i32 s2, s2, s7
	s_cmp_ge_u32 s3, s34
	s_cselect_b32 s7, s34, 0
	s_sub_i32 s3, s3, s7
	s_cmp_ge_u32 s3, s34
	s_cselect_b32 s7, s34, 0
	s_sub_i32 s3, s3, s7
	v_lshl_add_u32 v156, s3, v215, v223
	global_load_dwordx4 v[156:159], v156, s[44:45]
	v_mad_u32_u24 v160, s3, v199, v202
	global_load_dwordx2 v[160:161], v160, s[44:45]
	v_lshl_add_u32 v162, s2, 7, v204
	global_load_dwordx4 v[162:165], v162, s[44:45]
	s_add_i32 s2, s23, s1
	s_add_i32 s3, s2, 4
	s_add_i32 s2, s2, 2
	s_cmp_ge_u32 s2, s34
	s_cselect_b32 s7, s34, 0
	s_sub_i32 s2, s2, s7
	s_cmp_ge_u32 s3, s34
	s_cselect_b32 s7, s34, 0
	s_sub_i32 s3, s3, s7
	s_cmp_ge_u32 s3, s34
	s_cselect_b32 s7, s34, 0
	s_sub_i32 s3, s3, s7
	s_mov_b32 s12, s3
	s_mov_b32 s13, s2
	s_waitcnt lgkmcnt(4)
	v_mfma_f32_32x32x16_bf16 v[84:99], v[166:169], v[132:135], 0
	ds_read_b128 v[166:169], v205 offset:20032
	v_exp_f32_e32 v20, v20
	v_exp_f32_e32 v4, v4
	v_exp_f32_e32 v21, v21
	v_add_f32_e32 v179, v4, v20
	v_exp_f32_e32 v5, v5
	s_waitcnt lgkmcnt(4)
	v_mfma_f32_32x32x16_bf16 v[68:83], v[170:173], v[132:135], 0
	ds_read_b128 v[170:173], v205 offset:13408
	v_add_f32_e32 v179, v21, v179
	v_cvt_pk_bf16_f32 v100, v20, v21
	v_exp_f32_e32 v22, v22
	v_add_f32_e32 v179, v5, v179
	v_exp_f32_e32 v6, v6
	v_add_f32_e32 v179, v22, v179
	v_cvt_pk_bf16_f32 v108, v4, v5
	s_waitcnt lgkmcnt(4)
	v_mfma_f32_32x32x16_bf16 v[84:99], v[174:177], v[136:139], v[84:99]
	ds_read_b128 v[174:177], v205 offset:20064
	v_exp_f32_e32 v23, v23
	v_add_f32_e32 v179, v6, v179
	v_exp_f32_e32 v7, v7
	v_add_f32_e32 v179, v23, v179
	v_cvt_pk_bf16_f32 v101, v22, v23
	v_exp_f32_e32 v24, v24
	v_add_f32_e32 v179, v7, v179
	s_waitcnt lgkmcnt(4)
	v_mfma_f32_32x32x16_bf16 v[68:83], v[206:209], v[136:139], v[68:83]
	ds_read_b128 v[206:209], v205 offset:13440
	v_exp_f32_e32 v8, v8
	v_add_f32_e32 v179, v24, v179
	v_cvt_pk_bf16_f32 v109, v6, v7
	v_exp_f32_e32 v25, v25
	v_add_f32_e32 v179, v8, v179
	v_exp_f32_e32 v9, v9
	s_waitcnt lgkmcnt(4)
	v_mfma_f32_32x32x16_bf16 v[84:99], v[226:229], v[140:143], v[84:99]
	ds_read_b128 v[226:229], v205 offset:20096
	s_waitcnt vmcnt(3)
	ds_write_b128 v219, v[230:233] offset:45056
	ds_write_b64 v220, v[234:235] offset:45056
	v_add_f32_e32 v179, v25, v179
	v_cvt_pk_bf16_f32 v102, v24, v25
	v_exp_f32_e32 v26, v26
	v_add_f32_e32 v179, v9, v179
	v_exp_f32_e32 v10, v10
	v_add_f32_e32 v179, v26, v179
	v_cvt_pk_bf16_f32 v110, v8, v9
	s_waitcnt lgkmcnt(6)
	v_mfma_f32_32x32x16_bf16 v[68:83], v[166:169], v[140:143], v[68:83]
	ds_read_b128 v[166:169], v205 offset:13472
	v_exp_f32_e32 v27, v27
	v_add_f32_e32 v179, v10, v179
	v_exp_f32_e32 v11, v11
	v_add_f32_e32 v179, v27, v179
	v_cvt_pk_bf16_f32 v103, v26, v27
	v_exp_f32_e32 v28, v28
	v_add_f32_e32 v179, v11, v179
	s_waitcnt lgkmcnt(6)
	v_mfma_f32_32x32x16_bf16 v[84:99], v[170:173], v[144:147], v[84:99]
	ds_read_b128 v[170:173], v205 offset:20128
	v_exp_f32_e32 v29, v29
	v_add_f32_e32 v179, v28, v179
	v_cvt_pk_bf16_f32 v111, v10, v11
	v_exp_f32_e32 v30, v30
	v_add_f32_e32 v179, v29, v179
	v_exp_f32_e32 v31, v31
	s_waitcnt lgkmcnt(6)
	v_mfma_f32_32x32x16_bf16 v[68:83], v[174:177], v[144:147], v[68:83]
	v_add_f32_e32 v179, v30, v179
	v_cvt_pk_bf16_f32 v104, v28, v29
	v_exp_f32_e32 v32, v32
	v_add_f32_e32 v179, v31, v179
	v_exp_f32_e32 v33, v33
	v_add_f32_e32 v179, v32, v179
	v_cvt_pk_bf16_f32 v105, v30, v31
	s_waitcnt lgkmcnt(5)
	v_mfma_f32_32x32x16_bf16 v[84:99], v[206:209], v[148:151], v[84:99]
	s_waitcnt vmcnt(0)
	ds_write_b128 v219, v[156:159] offset:0
	ds_write_b64 v220, v[160:161] offset:0
	ds_write_b64 v221, v[162:163] offset:35840
	ds_write_b64 v222, v[164:165] offset:35840
	v_lshl_add_u32 v156, s12, v215, v223
	global_load_dwordx4 v[156:159], v156, s[44:45]
	v_mad_u32_u24 v160, s12, v199, v202
	global_load_dwordx2 v[160:161], v160, s[44:45]
	v_lshl_add_u32 v162, s13, 7, v204
	global_load_dwordx4 v[162:165], v162, s[44:45]
	s_add_i32 s12, s12, 1
	s_cmp_eq_u32 s12, s34
	s_cselect_b32 s12, 0, s12
	s_add_i32 s13, s13, 1
	s_cmp_eq_u32 s13, s34
	s_cselect_b32 s13, 0, s13
	v_exp_f32_e32 v34, v34
	v_add_f32_e32 v179, v33, v179
	v_exp_f32_e32 v35, v35
	v_add_f32_e32 v179, v34, v179
	v_cvt_pk_bf16_f32 v106, v32, v33
	v_exp_f32_e32 v12, v12
	v_add_f32_e32 v179, v35, v179
	s_waitcnt lgkmcnt(8)
	v_mfma_f32_32x32x16_bf16 v[68:83], v[226:229], v[148:151], v[68:83]
	v_exp_f32_e32 v13, v13
	v_add_f32_e32 v179, v12, v179
	v_cvt_pk_bf16_f32 v107, v34, v35
	v_exp_f32_e32 v14, v14
	v_add_f32_e32 v179, v13, v179
	v_exp_f32_e32 v15, v15
	s_waitcnt lgkmcnt(5)
	v_mfma_f32_32x32x16_bf16 v[84:99], v[166:169], v[152:155], v[84:99]
	v_add_f32_e32 v179, v14, v179
	v_cvt_pk_bf16_f32 v112, v12, v13
	v_exp_f32_e32 v16, v16
	v_add_f32_e32 v179, v15, v179
	v_exp_f32_e32 v17, v17
	v_add_f32_e32 v179, v16, v179
	v_cvt_pk_bf16_f32 v113, v14, v15
	s_waitcnt lgkmcnt(4)
	v_mfma_f32_32x32x16_bf16 v[68:83], v[170:173], v[152:155], v[68:83]
	v_exp_f32_e32 v18, v18
	v_add_f32_e32 v179, v17, v179
	v_exp_f32_e32 v19, v19
	v_add_f32_e32 v179, v18, v179
	v_cvt_pk_bf16_f32 v114, v16, v17
	v_add_f32_e32 v179, v19, v179
	v_cvt_pk_bf16_f32 v115, v18, v19
	v_add_f32_e32 v224, v224, v179
	s_add_i32 s1, s1, 1
	s_waitcnt lgkmcnt(0)
	s_barrier
	ds_read_b128 v[166:169], v205 offset:45056
	ds_read_b128 v[170:173], v205 offset:51712
	ds_read_b128 v[174:177], v205 offset:45088
	ds_read_b128 v[206:209], v205 offset:51744
	ds_read_b128 v[226:229], v205 offset:45120
	s_waitcnt lgkmcnt(0)
.Latt_u6_top:
	s_waitcnt lgkmcnt(4)
	v_mfma_f32_32x32x16_bf16 v[20:35], v[166:169], v[132:135], 0
	ds_read_b128 v[166:169], v205 offset:51776
	v_exp_f32_e32 v84, v84
	v_exp_f32_e32 v68, v68
	v_exp_f32_e32 v85, v85
	s_waitcnt lgkmcnt(4)
	v_mfma_f32_32x32x16_bf16 v[4:19], v[170:173], v[132:135], 0
	ds_read_b128 v[170:173], v205 offset:45152
	v_add_f32_e32 v179, v68, v84
	v_exp_f32_e32 v69, v69
	v_add_f32_e32 v179, v85, v179
	v_cvt_pk_bf16_f32 v116, v84, v85
	s_waitcnt lgkmcnt(4)
	v_mfma_f32_32x32x16_bf16 v[20:35], v[174:177], v[136:139], v[20:35]
	ds_read_b128 v[174:177], v205 offset:51808
	v_exp_f32_e32 v86, v86
	v_add_f32_e32 v179, v69, v179
	v_exp_f32_e32 v70, v70
	v_add_f32_e32 v179, v86, v179
	s_waitcnt lgkmcnt(4)
	v_mfma_f32_32x32x16_bf16 v[4:19], v[206:209], v[136:139], v[4:19]
	ds_read_b128 v[206:209], v205 offset:45184
	v_cvt_pk_bf16_f32 v124, v68, v69
	v_exp_f32_e32 v87, v87
	v_add_f32_e32 v179, v70, v179
	v_exp_f32_e32 v71, v71
	s_waitcnt lgkmcnt(4)
	v_mfma_f32_32x32x16_bf16 v[20:35], v[226:229], v[140:143], v[20:35]
	ds_read_b128 v[226:229], v205 offset:51840
	v_add_f32_e32 v179, v87, v179
	v_cvt_pk_bf16_f32 v117, v86, v87
	v_exp_f32_e32 v88, v88
	v_add_f32_e32 v179, v71, v179
	s_waitcnt lgkmcnt(4)
	v_mfma_f32_32x32x16_bf16 v[4:19], v[166:169], v[140:143], v[4:19]
	ds_read_b128 v[166:169], v205 offset:45216
	v_exp_f32_e32 v72, v72
	v_add_f32_e32 v179, v88, v179
	v_cvt_pk_bf16_f32 v125, v70, v71
	v_exp_f32_e32 v89, v89
	s_waitcnt lgkmcnt(4)
	v_mfma_f32_32x32x16_bf16 v[20:35], v[170:173], v[144:147], v[20:35]
	ds_read_b128 v[170:173], v205 offset:51872
	v_add_f32_e32 v179, v72, v179
	v_exp_f32_e32 v73, v73
	v_add_f32_e32 v179, v89, v179
	v_cvt_pk_bf16_f32 v118, v88, v89
	s_waitcnt lgkmcnt(4)
	v_mfma_f32_32x32x16_bf16 v[4:19], v[174:177], v[144:147], v[4:19]
	ds_read_b128 v[174:177], v178 offset:26624
	v_exp_f32_e32 v90, v90
	v_add_f32_e32 v179, v73, v179
	v_exp_f32_e32 v74, v74
	v_add_f32_e32 v179, v90, v179
	s_waitcnt lgkmcnt(4)
	v_mfma_f32_32x32x16_bf16 v[20:35], v[206:209], v[148:151], v[20:35]
	ds_read_b128 v[206:209], v178 offset:31232
	s_waitcnt vmcnt(0)
	ds_write_b128 v219, v[156:159] offset:13312
	v_cvt_pk_bf16_f32 v126, v72, v73
	v_exp_f32_e32 v91, v91
	v_add_f32_e32 v179, v74, v179
	v_exp_f32_e32 v75, v75
	s_waitcnt lgkmcnt(5)
	v_mfma_f32_32x32x16_bf16 v[4:19], v[226:229], v[148:151], v[4:19]
	ds_read_b128 v[226:229], v178 offset:26656
	ds_write_b64 v220, v[160:161] offset:13312
	v_add_f32_e32 v179, v91, v179
	v_cvt_pk_bf16_f32 v119, v90, v91
	v_exp_f32_e32 v92, v92
	v_add_f32_e32 v179, v75, v179
	s_waitcnt lgkmcnt(6)
	v_mfma_f32_32x32x16_bf16 v[20:35], v[166:169], v[152:155], v[20:35]
	ds_read_b128 v[166:169], v178 offset:31264
	ds_write_b64 v221, v[162:163] offset:58368
	v_exp_f32_e32 v93, v93
	v_add_f32_e32 v179, v92, v179
	v_cvt_pk_bf16_f32 v127, v74, v75
	v_exp_f32_e32 v94, v94
	s_waitcnt lgkmcnt(7)
	v_mfma_f32_32x32x16_bf16 v[4:19], v[170:173], v[152:155], v[4:19]
	ds_read_b128 v[170:173], v178 offset:26688
	ds_write_b64 v222, v[164:165] offset:58368
	v_add_f32_e32 v179, v93, v179
	v_exp_f32_e32 v95, v95
	v_add_f32_e32 v179, v94, v179
	v_cvt_pk_bf16_f32 v120, v92, v93
	s_waitcnt lgkmcnt(8)
	v_mfma_f32_32x32x16_bf16 v[36:51], v[174:177], v[100:103], v[36:51]
	ds_read_b128 v[174:177], v178 offset:31296
	v_lshl_add_u32 v156, s12, v215, v223
	global_load_dwordx4 v[156:159], v156, s[44:45]
	v_exp_f32_e32 v96, v96
	v_add_f32_e32 v179, v95, v179
	v_exp_f32_e32 v97, v97
	v_add_f32_e32 v179, v96, v179
	s_waitcnt lgkmcnt(8)
	v_mfma_f32_32x32x16_bf16 v[52:67], v[206:209], v[100:103], v[52:67]
	ds_read_b128 v[206:209], v178 offset:26720
	v_mad_u32_u24 v160, s12, v199, v202
	global_load_dwordx2 v[160:161], v160, s[44:45]
	s_add_i32 s12, s12, 1
	s_cmp_eq_u32 s12, s34
	s_cselect_b32 s12, 0, s12
	v_cvt_pk_bf16_f32 v121, v94, v95
	v_exp_f32_e32 v98, v98
	v_add_f32_e32 v179, v97, v179
	v_exp_f32_e32 v99, v99
	s_waitcnt lgkmcnt(7)
	v_mfma_f32_32x32x16_bf16 v[36:51], v[226:229], v[104:107], v[36:51]
	ds_read_b128 v[226:229], v178 offset:31328
	v_lshl_add_u32 v162, s13, 7, v204
	global_load_dwordx4 v[162:165], v162, s[44:45]
	s_add_i32 s13, s13, 1
	s_cmp_eq_u32 s13, s34
	s_cselect_b32 s13, 0, s13
	v_add_f32_e32 v179, v98, v179
	v_cvt_pk_bf16_f32 v122, v96, v97
	v_exp_f32_e32 v76, v76
	v_add_f32_e32 v179, v99, v179
	s_waitcnt lgkmcnt(6)
	v_mfma_f32_32x32x16_bf16 v[52:67], v[166:169], v[104:107], v[52:67]
	ds_read_b128 v[166:169], v205
	v_exp_f32_e32 v77, v77
	v_add_f32_e32 v179, v76, v179
	v_cvt_pk_bf16_f32 v123, v98, v99
	v_exp_f32_e32 v78, v78
	s_waitcnt lgkmcnt(5)
	v_mfma_f32_32x32x16_bf16 v[36:51], v[170:173], v[108:111], v[36:51]
	ds_read_b128 v[170:173], v205 offset:6656
	v_add_f32_e32 v179, v77, v179
	v_exp_f32_e32 v79, v79
	v_add_f32_e32 v179, v78, v179
	v_cvt_pk_bf16_f32 v128, v76, v77
	s_waitcnt lgkmcnt(4)
	v_mfma_f32_32x32x16_bf16 v[52:67], v[174:177], v[108:111], v[52:67]
	ds_read_b128 v[174:177], v205 offset:32
	v_exp_f32_e32 v80, v80
	v_add_f32_e32 v179, v79, v179
	v_exp_f32_e32 v81, v81
	v_add_f32_e32 v179, v80, v179
	s_waitcnt lgkmcnt(4)
	v_mfma_f32_32x32x16_bf16 v[36:51], v[206:209], v[112:115], v[36:51]
	ds_read_b128 v[206:209], v205 offset:6688
	v_cvt_pk_bf16_f32 v129, v78, v79
	v_exp_f32_e32 v82, v82
	v_add_f32_e32 v179, v81, v179
	v_exp_f32_e32 v83, v83
	s_waitcnt lgkmcnt(4)
	v_mfma_f32_32x32x16_bf16 v[52:67], v[226:229], v[112:115], v[52:67]
	ds_read_b128 v[226:229], v205 offset:64
	v_add_f32_e32 v179, v82, v179
	v_cvt_pk_bf16_f32 v130, v80, v81
	v_add_f32_e32 v179, v83, v179
	v_cvt_pk_bf16_f32 v131, v82, v83
	v_add_f32_e32 v224, v224, v179
	s_add_i32 s1, s1, 1
	s_cmp_lt_u32 s1, s34
	s_barrier
	s_cbranch_scc0 .Latt_u6_fin1
	s_waitcnt lgkmcnt(4)
	v_mfma_f32_32x32x16_bf16 v[84:99], v[166:169], v[132:135], 0
	ds_read_b128 v[166:169], v205 offset:6720
	v_exp_f32_e32 v20, v20
	v_exp_f32_e32 v4, v4
	v_exp_f32_e32 v21, v21
	s_waitcnt lgkmcnt(4)
	v_mfma_f32_32x32x16_bf16 v[68:83], v[170:173], v[132:135], 0
	ds_read_b128 v[170:173], v205 offset:96
	v_add_f32_e32 v179, v4, v20
	v_exp_f32_e32 v5, v5
	v_add_f32_e32 v179, v21, v179
	v_cvt_pk_bf16_f32 v100, v20, v21
	s_waitcnt lgkmcnt(4)
	v_mfma_f32_32x32x16_bf16 v[84:99], v[174:177], v[136:139], v[84:99]
	ds_read_b128 v[174:177], v205 offset:6752
	v_exp_f32_e32 v22, v22
	v_add_f32_e32 v179, v5, v179
	v_exp_f32_e32 v6, v6
	v_add_f32_e32 v179, v22, v179
	s_waitcnt lgkmcnt(4)
	v_mfma_f32_32x32x16_bf16 v[68:83], v[206:209], v[136:139], v[68:83]
	ds_read_b128 v[206:209], v205 offset:128
	v_cvt_pk_bf16_f32 v108, v4, v5
	v_exp_f32_e32 v23, v23
	v_add_f32_e32 v179, v6, v179
	v_exp_f32_e32 v7, v7
	s_waitcnt lgkmcnt(4)
	v_mfma_f32_32x32x16_bf16 v[84:99], v[226:229], v[140:143], v[84:99]
	ds_read_b128 v[226:229], v205 offset:6784
	v_add_f32_e32 v179, v23, v179
	v_cvt_pk_bf16_f32 v101, v22, v23
	v_exp_f32_e32 v24, v24
	v_add_f32_e32 v179, v7, v179
	s_waitcnt lgkmcnt(4)
	v_mfma_f32_32x32x16_bf16 v[68:83], v[166:169], v[140:143], v[68:83]
	ds_read_b128 v[166:169], v205 offset:160
	v_exp_f32_e32 v8, v8
	v_add_f32_e32 v179, v24, v179
	v_cvt_pk_bf16_f32 v109, v6, v7
	v_exp_f32_e32 v25, v25
	s_waitcnt lgkmcnt(4)
	v_mfma_f32_32x32x16_bf16 v[84:99], v[170:173], v[144:147], v[84:99]
	ds_read_b128 v[170:173], v205 offset:6816
	v_add_f32_e32 v179, v8, v179
	v_exp_f32_e32 v9, v9
	v_add_f32_e32 v179, v25, v179
	v_cvt_pk_bf16_f32 v102, v24, v25
	s_waitcnt lgkmcnt(4)
	v_mfma_f32_32x32x16_bf16 v[68:83], v[174:177], v[144:147], v[68:83]
	ds_read_b128 v[174:177], v178 offset:35840
	v_exp_f32_e32 v26, v26
	v_add_f32_e32 v179, v9, v179
	v_exp_f32_e32 v10, v10
	v_add_f32_e32 v179, v26, v179
	s_waitcnt lgkmcnt(4)
	v_mfma_f32_32x32x16_bf16 v[84:99], v[206:209], v[148:151], v[84:99]
	ds_read_b128 v[206:209], v178 offset:40448
	s_waitcnt vmcnt(0)
	ds_write_b128 v219, v[156:159] offset:45056
	v_cvt_pk_bf16_f32 v110, v8, v9
	v_exp_f32_e32 v27, v27
	v_add_f32_e32 v179, v10, v179
	v_exp_f32_e32 v11, v11
	s_waitcnt lgkmcnt(5)
	v_mfma_f32_32x32x16_bf16 v[68:83], v[226:229], v[148:151], v[68:83]
	ds_read_b128 v[226:229], v178 offset:35872
	ds_write_b64 v220, v[160:161] offset:45056
	v_add_f32_e32 v179, v27, v179
	v_cvt_pk_bf16_f32 v103, v26, v27
	v_exp_f32_e32 v28, v28
	v_add_f32_e32 v179, v11, v179
	s_waitcnt lgkmcnt(6)
	v_mfma_f32_32x32x16_bf16 v[84:99], v[166:169], v[152:155], v[84:99]
	ds_read_b128 v[166:169], v178 offset:40480
	ds_write_b64 v221, v[162:163] offset:26624
	v_exp_f32_e32 v29, v29
	v_add_f32_e32 v179, v28, v179
	v_cvt_pk_bf16_f32 v111, v10, v11
	v_exp_f32_e32 v30, v30
	s_waitcnt lgkmcnt(7)
	v_mfma_f32_32x32x16_bf16 v[68:83], v[170:173], v[152:155], v[68:83]
	ds_read_b128 v[170:173], v178 offset:35904
	ds_write_b64 v222, v[164:165] offset:26624
	v_add_f32_e32 v179, v29, v179
	v_exp_f32_e32 v31, v31
	v_add_f32_e32 v179, v30, v179
	v_cvt_pk_bf16_f32 v104, v28, v29
	s_waitcnt lgkmcnt(8)
	v_mfma_f32_32x32x16_bf16 v[36:51], v[174:177], v[116:119], v[36:51]
	ds_read_b128 v[174:177], v178 offset:40512
	v_lshl_add_u32 v156, s12, v215, v223
	global_load_dwordx4 v[156:159], v156, s[44:45]
	v_exp_f32_e32 v32, v32
	v_add_f32_e32 v179, v31, v179
	v_exp_f32_e32 v33, v33
	v_add_f32_e32 v179, v32, v179
	s_waitcnt lgkmcnt(8)
	v_mfma_f32_32x32x16_bf16 v[52:67], v[206:209], v[116:119], v[52:67]
	ds_read_b128 v[206:209], v178 offset:35936
	v_mad_u32_u24 v160, s12, v199, v202
	global_load_dwordx2 v[160:161], v160, s[44:45]
	s_add_i32 s12, s12, 1
	s_cmp_eq_u32 s12, s34
	s_cselect_b32 s12, 0, s12
	v_cvt_pk_bf16_f32 v105, v30, v31
	v_exp_f32_e32 v34, v34
	v_add_f32_e32 v179, v33, v179
	v_exp_f32_e32 v35, v35
	s_waitcnt lgkmcnt(7)
	v_mfma_f32_32x32x16_bf16 v[36:51], v[226:229], v[120:123], v[36:51]
	ds_read_b128 v[226:229], v178 offset:40544
	v_lshl_add_u32 v162, s13, 7, v204
	global_load_dwordx4 v[162:165], v162, s[44:45]
	s_add_i32 s13, s13, 1
	s_cmp_eq_u32 s13, s34
	s_cselect_b32 s13, 0, s13
	v_add_f32_e32 v179, v34, v179
	v_cvt_pk_bf16_f32 v106, v32, v33
	v_exp_f32_e32 v12, v12
	v_add_f32_e32 v179, v35, v179
	s_waitcnt lgkmcnt(6)
	v_mfma_f32_32x32x16_bf16 v[52:67], v[166:169], v[120:123], v[52:67]
	ds_read_b128 v[166:169], v205 offset:13312
	v_exp_f32_e32 v13, v13
	v_add_f32_e32 v179, v12, v179
	v_cvt_pk_bf16_f32 v107, v34, v35
	v_exp_f32_e32 v14, v14
	s_waitcnt lgkmcnt(5)
	v_mfma_f32_32x32x16_bf16 v[36:51], v[170:173], v[124:127], v[36:51]
	ds_read_b128 v[170:173], v205 offset:19968
	v_add_f32_e32 v179, v13, v179
	v_exp_f32_e32 v15, v15
	v_add_f32_e32 v179, v14, v179
	v_cvt_pk_bf16_f32 v112, v12, v13
	s_waitcnt lgkmcnt(4)
	v_mfma_f32_32x32x16_bf16 v[52:67], v[174:177], v[124:127], v[52:67]
	ds_read_b128 v[174:177], v205 offset:13344
	v_exp_f32_e32 v16, v16
	v_add_f32_e32 v179, v15, v179
	v_exp_f32_e32 v17, v17
	v_add_f32_e32 v179, v16, v179
	s_waitcnt lgkmcnt(4)
	v_mfma_f32_32x32x16_bf16 v[36:51], v[206:209], v[128:131], v[36:51]
	ds_read_b128 v[206:209], v205 offset:20000
	v_cvt_pk_bf16_f32 v113, v14, v15
	v_exp_f32_e32 v18, v18
	v_add_f32_e32 v179, v17, v179
	v_exp_f32_e32 v19, v19
	s_waitcnt lgkmcnt(4)
	v_mfma_f32_32x32x16_bf16 v[52:67], v[226:229], v[128:131], v[52:67]
	ds_read_b128 v[226:229], v205 offset:13376
	v_add_f32_e32 v179, v18, v179
	v_cvt_pk_bf16_f32 v114, v16, v17
	v_add_f32_e32 v179, v19, v179
	v_cvt_pk_bf16_f32 v115, v18, v19
	v_add_f32_e32 v224, v224, v179
	s_add_i32 s1, s1, 1
	s_barrier
	s_waitcnt lgkmcnt(4)
	v_mfma_f32_32x32x16_bf16 v[20:35], v[166:169], v[132:135], 0
	ds_read_b128 v[166:169], v205 offset:20032
	v_exp_f32_e32 v84, v84
	v_exp_f32_e32 v68, v68
	v_exp_f32_e32 v85, v85
	s_waitcnt lgkmcnt(4)
	v_mfma_f32_32x32x16_bf16 v[4:19], v[170:173], v[132:135], 0
	ds_read_b128 v[170:173], v205 offset:13408
	v_add_f32_e32 v179, v68, v84
	v_exp_f32_e32 v69, v69
	v_add_f32_e32 v179, v85, v179
	v_cvt_pk_bf16_f32 v116, v84, v85
	s_waitcnt lgkmcnt(4)
	v_mfma_f32_32x32x16_bf16 v[20:35], v[174:177], v[136:139], v[20:35]
	ds_read_b128 v[174:177], v205 offset:20064
	v_exp_f32_e32 v86, v86
	v_add_f32_e32 v179, v69, v179
	v_exp_f32_e32 v70, v70
	v_add_f32_e32 v179, v86, v179
	s_waitcnt lgkmcnt(4)
	v_mfma_f32_32x32x16_bf16 v[4:19], v[206:209], v[136:139], v[4:19]
	ds_read_b128 v[206:209], v205 offset:13440
	v_cvt_pk_bf16_f32 v124, v68, v69
	v_exp_f32_e32 v87, v87
	v_add_f32_e32 v179, v70, v179
	v_exp_f32_e32 v71, v71
	s_waitcnt lgkmcnt(4)
	v_mfma_f32_32x32x16_bf16 v[20:35], v[226:229], v[140:143], v[20:35]
	ds_read_b128 v[226:229], v205 offset:20096
	v_add_f32_e32 v179, v87, v179
	v_cvt_pk_bf16_f32 v117, v86, v87
	v_exp_f32_e32 v88, v88
	v_add_f32_e32 v179, v71, v179
	s_waitcnt lgkmcnt(4)
	v_mfma_f32_32x32x16_bf16 v[4:19], v[166:169], v[140:143], v[4:19]
	ds_read_b128 v[166:169], v205 offset:13472
	v_exp_f32_e32 v72, v72
	v_add_f32_e32 v179, v88, v179
	v_cvt_pk_bf16_f32 v125, v70, v71
	v_exp_f32_e32 v89, v89
	s_waitcnt lgkmcnt(4)
	v_mfma_f32_32x32x16_bf16 v[20:35], v[170:173], v[144:147], v[20:35]
	ds_read_b128 v[170:173], v205 offset:20128
	v_add_f32_e32 v179, v72, v179
	v_exp_f32_e32 v73, v73
	v_add_f32_e32 v179, v89, v179
	v_cvt_pk_bf16_f32 v118, v88, v89
	s_waitcnt lgkmcnt(4)
	v_mfma_f32_32x32x16_bf16 v[4:19], v[174:177], v[144:147], v[4:19]
	ds_read_b128 v[174:177], v178 offset:58368
	v_exp_f32_e32 v90, v90
	v_add_f32_e32 v179, v73, v179
	v_exp_f32_e32 v74, v74
	v_add_f32_e32 v179, v90, v179
	s_waitcnt lgkmcnt(4)
	v_mfma_f32_32x32x16_bf16 v[20:35], v[206:209], v[148:151], v[20:35]
	ds_read_b128 v[206:209], v178 offset:62976
	s_waitcnt vmcnt(0)
	ds_write_b128 v219, v[156:159] offset:0
	v_cvt_pk_bf16_f32 v126, v72, v73
	v_exp_f32_e32 v91, v91
	v_add_f32_e32 v179, v74, v179
	v_exp_f32_e32 v75, v75
	s_waitcnt lgkmcnt(5)
	v_mfma_f32_32x32x16_bf16 v[4:19], v[226:229], v[148:151], v[4:19]
	ds_read_b128 v[226:229], v178 offset:58400
	ds_write_b64 v220, v[160:161] offset:0
	v_add_f32_e32 v179, v91, v179
	v_cvt_pk_bf16_f32 v119, v90, v91
	v_exp_f32_e32 v92, v92
	v_add_f32_e32 v179, v75, v179
	s_waitcnt lgkmcnt(6)
	v_mfma_f32_32x32x16_bf16 v[20:35], v[166:169], v[152:155], v[20:35]
	ds_read_b128 v[166:169], v178 offset:63008
	ds_write_b64 v221, v[162:163] offset:35840
	v_exp_f32_e32 v93, v93
	v_add_f32_e32 v179, v92, v179
	v_cvt_pk_bf16_f32 v127, v74, v75
	v_exp_f32_e32 v94, v94
	s_waitcnt lgkmcnt(7)
	v_mfma_f32_32x32x16_bf16 v[4:19], v[170:173], v[152:155], v[4:19]
	ds_read_b128 v[170:173], v178 offset:58432
	ds_write_b64 v222, v[164:165] offset:35840
	v_add_f32_e32 v179, v93, v179
	v_exp_f32_e32 v95, v95
	v_add_f32_e32 v179, v94, v179
	v_cvt_pk_bf16_f32 v120, v92, v93
	s_waitcnt lgkmcnt(8)
	v_mfma_f32_32x32x16_bf16 v[36:51], v[174:177], v[100:103], v[36:51]
	ds_read_b128 v[174:177], v178 offset:63040
	v_lshl_add_u32 v156, s12, v215, v223
	global_load_dwordx4 v[156:159], v156, s[44:45]
	v_exp_f32_e32 v96, v96
	v_add_f32_e32 v179, v95, v179
	v_exp_f32_e32 v97, v97
	v_add_f32_e32 v179, v96, v179
	s_waitcnt lgkmcnt(8)
	v_mfma_f32_32x32x16_bf16 v[52:67], v[206:209], v[100:103], v[52:67]
	ds_read_b128 v[206:209], v178 offset:58464
	v_mad_u32_u24 v160, s12, v199, v202
	global_load_dwordx2 v[160:161], v160, s[44:45]
	s_add_i32 s12, s12, 1
	s_cmp_eq_u32 s12, s34
	s_cselect_b32 s12, 0, s12
	v_cvt_pk_bf16_f32 v121, v94, v95
	v_exp_f32_e32 v98, v98
	v_add_f32_e32 v179, v97, v179
	v_exp_f32_e32 v99, v99
	s_waitcnt lgkmcnt(7)
	v_mfma_f32_32x32x16_bf16 v[36:51], v[226:229], v[104:107], v[36:51]
	ds_read_b128 v[226:229], v178 offset:63072
	v_lshl_add_u32 v162, s13, 7, v204
	global_load_dwordx4 v[162:165], v162, s[44:45]
	s_add_i32 s13, s13, 1
	s_cmp_eq_u32 s13, s34
	s_cselect_b32 s13, 0, s13
	v_add_f32_e32 v179, v98, v179
	v_cvt_pk_bf16_f32 v122, v96, v97
	v_exp_f32_e32 v76, v76
	v_add_f32_e32 v179, v99, v179
	s_waitcnt lgkmcnt(6)
	v_mfma_f32_32x32x16_bf16 v[52:67], v[166:169], v[104:107], v[52:67]
	ds_read_b128 v[166:169], v205 offset:45056
	v_exp_f32_e32 v77, v77
	v_add_f32_e32 v179, v76, v179
	v_cvt_pk_bf16_f32 v123, v98, v99
	v_exp_f32_e32 v78, v78
	s_waitcnt lgkmcnt(5)
	v_mfma_f32_32x32x16_bf16 v[36:51], v[170:173], v[108:111], v[36:51]
	ds_read_b128 v[170:173], v205 offset:51712
	v_add_f32_e32 v179, v77, v179
	v_exp_f32_e32 v79, v79
	v_add_f32_e32 v179, v78, v179
	v_cvt_pk_bf16_f32 v128, v76, v77
	s_waitcnt lgkmcnt(4)
	v_mfma_f32_32x32x16_bf16 v[52:67], v[174:177], v[108:111], v[52:67]
	ds_read_b128 v[174:177], v205 offset:45088
	v_exp_f32_e32 v80, v80
	v_add_f32_e32 v179, v79, v179
	v_exp_f32_e32 v81, v81
	v_add_f32_e32 v179, v80, v179
	s_waitcnt lgkmcnt(4)
	v_mfma_f32_32x32x16_bf16 v[36:51], v[206:209], v[112:115], v[36:51]
	ds_read_b128 v[206:209], v205 offset:51744
	v_cvt_pk_bf16_f32 v129, v78, v79
	v_exp_f32_e32 v82, v82
	v_add_f32_e32 v179, v81, v179
	v_exp_f32_e32 v83, v83
	s_waitcnt lgkmcnt(4)
	v_mfma_f32_32x32x16_bf16 v[52:67], v[226:229], v[112:115], v[52:67]
	ds_read_b128 v[226:229], v205 offset:45120
	v_add_f32_e32 v179, v82, v179
	v_cvt_pk_bf16_f32 v130, v80, v81
	v_add_f32_e32 v179, v83, v179
	v_cvt_pk_bf16_f32 v131, v82, v83
	v_add_f32_e32 v224, v224, v179
	s_add_i32 s1, s1, 1
	s_cmp_lt_u32 s1, s34
	s_barrier
	s_cbranch_scc0 .Latt_u6_fin0
	s_waitcnt lgkmcnt(4)
	v_mfma_f32_32x32x16_bf16 v[84:99], v[166:169], v[132:135], 0
	ds_read_b128 v[166:169], v205 offset:51776
	v_exp_f32_e32 v20, v20
	v_exp_f32_e32 v4, v4
	v_exp_f32_e32 v21, v21
	s_waitcnt lgkmcnt(4)
	v_mfma_f32_32x32x16_bf16 v[68:83], v[170:173], v[132:135], 0
	ds_read_b128 v[170:173], v205 offset:45152
	v_add_f32_e32 v179, v4, v20
	v_exp_f32_e32 v5, v5
	v_add_f32_e32 v179, v21, v179
	v_cvt_pk_bf16_f32 v100, v20, v21
	s_waitcnt lgkmcnt(4)
	v_mfma_f32_32x32x16_bf16 v[84:99], v[174:177], v[136:139], v[84:99]
	ds_read_b128 v[174:177], v205 offset:51808
	v_exp_f32_e32 v22, v22
	v_add_f32_e32 v179, v5, v179
	v_exp_f32_e32 v6, v6
	v_add_f32_e32 v179, v22, v179
	s_waitcnt lgkmcnt(4)
	v_mfma_f32_32x32x16_bf16 v[68:83], v[206:209], v[136:139], v[68:83]
	ds_read_b128 v[206:209], v205 offset:45184
	v_cvt_pk_bf16_f32 v108, v4, v5
	v_exp_f32_e32 v23, v23
	v_add_f32_e32 v179, v6, v179
	v_exp_f32_e32 v7, v7
	s_waitcnt lgkmcnt(4)
	v_mfma_f32_32x32x16_bf16 v[84:99], v[226:229], v[140:143], v[84:99]
	ds_read_b128 v[226:229], v205 offset:51840
	v_add_f32_e32 v179, v23, v179
	v_cvt_pk_bf16_f32 v101, v22, v23
	v_exp_f32_e32 v24, v24
	v_add_f32_e32 v179, v7, v179
	s_waitcnt lgkmcnt(4)
	v_mfma_f32_32x32x16_bf16 v[68:83], v[166:169], v[140:143], v[68:83]
	ds_read_b128 v[166:169], v205 offset:45216
	v_exp_f32_e32 v8, v8
	v_add_f32_e32 v179, v24, v179
	v_cvt_pk_bf16_f32 v109, v6, v7
	v_exp_f32_e32 v25, v25
	s_waitcnt lgkmcnt(4)
	v_mfma_f32_32x32x16_bf16 v[84:99], v[170:173], v[144:147], v[84:99]
	ds_read_b128 v[170:173], v205 offset:51872
	v_add_f32_e32 v179, v8, v179
	v_exp_f32_e32 v9, v9
	v_add_f32_e32 v179, v25, v179
	v_cvt_pk_bf16_f32 v102, v24, v25
	s_waitcnt lgkmcnt(4)
	v_mfma_f32_32x32x16_bf16 v[68:83], v[174:177], v[144:147], v[68:83]
	ds_read_b128 v[174:177], v178 offset:26624
	v_exp_f32_e32 v26, v26
	v_add_f32_e32 v179, v9, v179
	v_exp_f32_e32 v10, v10
	v_add_f32_e32 v179, v26, v179
	s_waitcnt lgkmcnt(4)
	v_mfma_f32_32x32x16_bf16 v[84:99], v[206:209], v[148:151], v[84:99]
	ds_read_b128 v[206:209], v178 offset:31232
	s_waitcnt vmcnt(0)
	ds_write_b128 v219, v[156:159] offset:13312
	v_cvt_pk_bf16_f32 v110, v8, v9
	v_exp_f32_e32 v27, v27
	v_add_f32_e32 v179, v10, v179
	v_exp_f32_e32 v11, v11
	s_waitcnt lgkmcnt(5)
	v_mfma_f32_32x32x16_bf16 v[68:83], v[226:229], v[148:151], v[68:83]
	ds_read_b128 v[226:229], v178 offset:26656
	ds_write_b64 v220, v[160:161] offset:13312
	v_add_f32_e32 v179, v27, v179
	v_cvt_pk_bf16_f32 v103, v26, v27
	v_exp_f32_e32 v28, v28
	v_add_f32_e32 v179, v11, v179
	s_waitcnt lgkmcnt(6)
	v_mfma_f32_32x32x16_bf16 v[84:99], v[166:169], v[152:155], v[84:99]
	ds_read_b128 v[166:169], v178 offset:31264
	ds_write_b64 v221, v[162:163] offset:58368
	v_exp_f32_e32 v29, v29
	v_add_f32_e32 v179, v28, v179
	v_cvt_pk_bf16_f32 v111, v10, v11
	v_exp_f32_e32 v30, v30
	s_waitcnt lgkmcnt(7)
	v_mfma_f32_32x32x16_bf16 v[68:83], v[170:173], v[152:155], v[68:83]
	ds_read_b128 v[170:173], v178 offset:26688
	ds_write_b64 v222, v[164:165] offset:58368
	v_add_f32_e32 v179, v29, v179
	v_exp_f32_e32 v31, v31
	v_add_f32_e32 v179, v30, v179
	v_cvt_pk_bf16_f32 v104, v28, v29
	s_waitcnt lgkmcnt(8)
	v_mfma_f32_32x32x16_bf16 v[36:51], v[174:177], v[116:119], v[36:51]
	ds_read_b128 v[174:177], v178 offset:31296
	v_lshl_add_u32 v156, s12, v215, v223
	global_load_dwordx4 v[156:159], v156, s[44:45]
	v_exp_f32_e32 v32, v32
	v_add_f32_e32 v179, v31, v179
	v_exp_f32_e32 v33, v33
	v_add_f32_e32 v179, v32, v179
	s_waitcnt lgkmcnt(8)
	v_mfma_f32_32x32x16_bf16 v[52:67], v[206:209], v[116:119], v[52:67]
	ds_read_b128 v[206:209], v178 offset:26720
	v_mad_u32_u24 v160, s12, v199, v202
	global_load_dwordx2 v[160:161], v160, s[44:45]
	s_add_i32 s12, s12, 1
	s_cmp_eq_u32 s12, s34
	s_cselect_b32 s12, 0, s12
	v_cvt_pk_bf16_f32 v105, v30, v31
	v_exp_f32_e32 v34, v34
	v_add_f32_e32 v179, v33, v179
	v_exp_f32_e32 v35, v35
	s_waitcnt lgkmcnt(7)
	v_mfma_f32_32x32x16_bf16 v[36:51], v[226:229], v[120:123], v[36:51]
	ds_read_b128 v[226:229], v178 offset:31328
	v_lshl_add_u32 v162, s13, 7, v204
	global_load_dwordx4 v[162:165], v162, s[44:45]
	s_add_i32 s13, s13, 1
	s_cmp_eq_u32 s13, s34
	s_cselect_b32 s13, 0, s13
	v_add_f32_e32 v179, v34, v179
	v_cvt_pk_bf16_f32 v106, v32, v33
	v_exp_f32_e32 v12, v12
	v_add_f32_e32 v179, v35, v179
	s_waitcnt lgkmcnt(6)
	v_mfma_f32_32x32x16_bf16 v[52:67], v[166:169], v[120:123], v[52:67]
	ds_read_b128 v[166:169], v205
	v_exp_f32_e32 v13, v13
	v_add_f32_e32 v179, v12, v179
	v_cvt_pk_bf16_f32 v107, v34, v35
	v_exp_f32_e32 v14, v14
	s_waitcnt lgkmcnt(5)
	v_mfma_f32_32x32x16_bf16 v[36:51], v[170:173], v[124:127], v[36:51]
	ds_read_b128 v[170:173], v205 offset:6656
	v_add_f32_e32 v179, v13, v179
	v_exp_f32_e32 v15, v15
	v_add_f32_e32 v179, v14, v179
	v_cvt_pk_bf16_f32 v112, v12, v13
	s_waitcnt lgkmcnt(4)
	v_mfma_f32_32x32x16_bf16 v[52:67], v[174:177], v[124:127], v[52:67]
	ds_read_b128 v[174:177], v205 offset:32
	v_exp_f32_e32 v16, v16
	v_add_f32_e32 v179, v15, v179
	v_exp_f32_e32 v17, v17
	v_add_f32_e32 v179, v16, v179
	s_waitcnt lgkmcnt(4)
	v_mfma_f32_32x32x16_bf16 v[36:51], v[206:209], v[128:131], v[36:51]
	ds_read_b128 v[206:209], v205 offset:6688
	v_cvt_pk_bf16_f32 v113, v14, v15
	v_exp_f32_e32 v18, v18
	v_add_f32_e32 v179, v17, v179
	v_exp_f32_e32 v19, v19
	s_waitcnt lgkmcnt(4)
	v_mfma_f32_32x32x16_bf16 v[52:67], v[226:229], v[128:131], v[52:67]
	ds_read_b128 v[226:229], v205 offset:64
	v_add_f32_e32 v179, v18, v179
	v_cvt_pk_bf16_f32 v114, v16, v17
	v_add_f32_e32 v179, v19, v179
	v_cvt_pk_bf16_f32 v115, v18, v19
	v_add_f32_e32 v224, v224, v179
	s_add_i32 s1, s1, 1
	s_barrier
	s_waitcnt lgkmcnt(4)
	v_mfma_f32_32x32x16_bf16 v[20:35], v[166:169], v[132:135], 0
	ds_read_b128 v[166:169], v205 offset:6720
	v_exp_f32_e32 v84, v84
	v_exp_f32_e32 v68, v68
	v_exp_f32_e32 v85, v85
	s_waitcnt lgkmcnt(4)
	v_mfma_f32_32x32x16_bf16 v[4:19], v[170:173], v[132:135], 0
	ds_read_b128 v[170:173], v205 offset:96
	v_add_f32_e32 v179, v68, v84
	v_exp_f32_e32 v69, v69
	v_add_f32_e32 v179, v85, v179
	v_cvt_pk_bf16_f32 v116, v84, v85
	s_waitcnt lgkmcnt(4)
	v_mfma_f32_32x32x16_bf16 v[20:35], v[174:177], v[136:139], v[20:35]
	ds_read_b128 v[174:177], v205 offset:6752
	v_exp_f32_e32 v86, v86
	v_add_f32_e32 v179, v69, v179
	v_exp_f32_e32 v70, v70
	v_add_f32_e32 v179, v86, v179
	s_waitcnt lgkmcnt(4)
	v_mfma_f32_32x32x16_bf16 v[4:19], v[206:209], v[136:139], v[4:19]
	ds_read_b128 v[206:209], v205 offset:128
	v_cvt_pk_bf16_f32 v124, v68, v69
	v_exp_f32_e32 v87, v87
	v_add_f32_e32 v179, v70, v179
	v_exp_f32_e32 v71, v71
	s_waitcnt lgkmcnt(4)
	v_mfma_f32_32x32x16_bf16 v[20:35], v[226:229], v[140:143], v[20:35]
	ds_read_b128 v[226:229], v205 offset:6784
	v_add_f32_e32 v179, v87, v179
	v_cvt_pk_bf16_f32 v117, v86, v87
	v_exp_f32_e32 v88, v88
	v_add_f32_e32 v179, v71, v179
	s_waitcnt lgkmcnt(4)
	v_mfma_f32_32x32x16_bf16 v[4:19], v[166:169], v[140:143], v[4:19]
	ds_read_b128 v[166:169], v205 offset:160
	v_exp_f32_e32 v72, v72
	v_add_f32_e32 v179, v88, v179
	v_cvt_pk_bf16_f32 v125, v70, v71
	v_exp_f32_e32 v89, v89
	s_waitcnt lgkmcnt(4)
	v_mfma_f32_32x32x16_bf16 v[20:35], v[170:173], v[144:147], v[20:35]
	ds_read_b128 v[170:173], v205 offset:6816
	v_add_f32_e32 v179, v72, v179
	v_exp_f32_e32 v73, v73
	v_add_f32_e32 v179, v89, v179
	v_cvt_pk_bf16_f32 v118, v88, v89
	s_waitcnt lgkmcnt(4)
	v_mfma_f32_32x32x16_bf16 v[4:19], v[174:177], v[144:147], v[4:19]
	ds_read_b128 v[174:177], v178 offset:35840
	v_exp_f32_e32 v90, v90
	v_add_f32_e32 v179, v73, v179
	v_exp_f32_e32 v74, v74
	v_add_f32_e32 v179, v90, v179
	s_waitcnt lgkmcnt(4)
	v_mfma_f32_32x32x16_bf16 v[20:35], v[206:209], v[148:151], v[20:35]
	ds_read_b128 v[206:209], v178 offset:40448
	s_waitcnt vmcnt(0)
	ds_write_b128 v219, v[156:159] offset:45056
	v_cvt_pk_bf16_f32 v126, v72, v73
	v_exp_f32_e32 v91, v91
	v_add_f32_e32 v179, v74, v179
	v_exp_f32_e32 v75, v75
	s_waitcnt lgkmcnt(5)
	v_mfma_f32_32x32x16_bf16 v[4:19], v[226:229], v[148:151], v[4:19]
	ds_read_b128 v[226:229], v178 offset:35872
	ds_write_b64 v220, v[160:161] offset:45056
	v_add_f32_e32 v179, v91, v179
	v_cvt_pk_bf16_f32 v119, v90, v91
	v_exp_f32_e32 v92, v92
	v_add_f32_e32 v179, v75, v179
	s_waitcnt lgkmcnt(6)
	v_mfma_f32_32x32x16_bf16 v[20:35], v[166:169], v[152:155], v[20:35]
	ds_read_b128 v[166:169], v178 offset:40480
	ds_write_b64 v221, v[162:163] offset:26624
	v_exp_f32_e32 v93, v93
	v_add_f32_e32 v179, v92, v179
	v_cvt_pk_bf16_f32 v127, v74, v75
	v_exp_f32_e32 v94, v94
	s_waitcnt lgkmcnt(7)
	v_mfma_f32_32x32x16_bf16 v[4:19], v[170:173], v[152:155], v[4:19]
	ds_read_b128 v[170:173], v178 offset:35904
	ds_write_b64 v222, v[164:165] offset:26624
	v_add_f32_e32 v179, v93, v179
	v_exp_f32_e32 v95, v95
	v_add_f32_e32 v179, v94, v179
	v_cvt_pk_bf16_f32 v120, v92, v93
	s_waitcnt lgkmcnt(8)
	v_mfma_f32_32x32x16_bf16 v[36:51], v[174:177], v[100:103], v[36:51]
	ds_read_b128 v[174:177], v178 offset:40512
	v_lshl_add_u32 v156, s12, v215, v223
	global_load_dwordx4 v[156:159], v156, s[44:45]
	v_exp_f32_e32 v96, v96
	v_add_f32_e32 v179, v95, v179
	v_exp_f32_e32 v97, v97
	v_add_f32_e32 v179, v96, v179
	s_waitcnt lgkmcnt(8)
	v_mfma_f32_32x32x16_bf16 v[52:67], v[206:209], v[100:103], v[52:67]
	ds_read_b128 v[206:209], v178 offset:35936
	v_mad_u32_u24 v160, s12, v199, v202
	global_load_dwordx2 v[160:161], v160, s[44:45]
	s_add_i32 s12, s12, 1
	s_cmp_eq_u32 s12, s34
	s_cselect_b32 s12, 0, s12
	v_cvt_pk_bf16_f32 v121, v94, v95
	v_exp_f32_e32 v98, v98
	v_add_f32_e32 v179, v97, v179
	v_exp_f32_e32 v99, v99
	s_waitcnt lgkmcnt(7)
	v_mfma_f32_32x32x16_bf16 v[36:51], v[226:229], v[104:107], v[36:51]
	ds_read_b128 v[226:229], v178 offset:40544
	v_lshl_add_u32 v162, s13, 7, v204
	global_load_dwordx4 v[162:165], v162, s[44:45]
	s_add_i32 s13, s13, 1
	s_cmp_eq_u32 s13, s34
	s_cselect_b32 s13, 0, s13
	v_add_f32_e32 v179, v98, v179
	v_cvt_pk_bf16_f32 v122, v96, v97
	v_exp_f32_e32 v76, v76
	v_add_f32_e32 v179, v99, v179
	s_waitcnt lgkmcnt(6)
	v_mfma_f32_32x32x16_bf16 v[52:67], v[166:169], v[104:107], v[52:67]
	ds_read_b128 v[166:169], v205 offset:13312
	v_exp_f32_e32 v77, v77
	v_add_f32_e32 v179, v76, v179
	v_cvt_pk_bf16_f32 v123, v98, v99
	v_exp_f32_e32 v78, v78
	s_waitcnt lgkmcnt(5)
	v_mfma_f32_32x32x16_bf16 v[36:51], v[170:173], v[108:111], v[36:51]
	ds_read_b128 v[170:173], v205 offset:19968
	v_add_f32_e32 v179, v77, v179
	v_exp_f32_e32 v79, v79
	v_add_f32_e32 v179, v78, v179
	v_cvt_pk_bf16_f32 v128, v76, v77
	s_waitcnt lgkmcnt(4)
	v_mfma_f32_32x32x16_bf16 v[52:67], v[174:177], v[108:111], v[52:67]
	ds_read_b128 v[174:177], v205 offset:13344
	v_exp_f32_e32 v80, v80
	v_add_f32_e32 v179, v79, v179
	v_exp_f32_e32 v81, v81
	v_add_f32_e32 v179, v80, v179
	s_waitcnt lgkmcnt(4)
	v_mfma_f32_32x32x16_bf16 v[36:51], v[206:209], v[112:115], v[36:51]
	ds_read_b128 v[206:209], v205 offset:20000
	v_cvt_pk_bf16_f32 v129, v78, v79
	v_exp_f32_e32 v82, v82
	v_add_f32_e32 v179, v81, v179
	v_exp_f32_e32 v83, v83
	s_waitcnt lgkmcnt(4)
	v_mfma_f32_32x32x16_bf16 v[52:67], v[226:229], v[112:115], v[52:67]
	ds_read_b128 v[226:229], v205 offset:13376
	v_add_f32_e32 v179, v82, v179
	v_cvt_pk_bf16_f32 v130, v80, v81
	v_add_f32_e32 v179, v83, v179
	v_cvt_pk_bf16_f32 v131, v82, v83
	v_add_f32_e32 v224, v224, v179
	s_add_i32 s1, s1, 1
	s_cmp_lt_u32 s1, s34
	s_barrier
	s_cbranch_scc0 .Latt_u6_fin2
	s_waitcnt lgkmcnt(4)
	v_mfma_f32_32x32x16_bf16 v[84:99], v[166:169], v[132:135], 0
	ds_read_b128 v[166:169], v205 offset:20032
	v_exp_f32_e32 v20, v20
	v_exp_f32_e32 v4, v4
	v_exp_f32_e32 v21, v21
	s_waitcnt lgkmcnt(4)
	v_mfma_f32_32x32x16_bf16 v[68:83], v[170:173], v[132:135], 0
	ds_read_b128 v[170:173], v205 offset:13408
	v_add_f32_e32 v179, v4, v20
	v_exp_f32_e32 v5, v5
	v_add_f32_e32 v179, v21, v179
	v_cvt_pk_bf16_f32 v100, v20, v21
	s_waitcnt lgkmcnt(4)
	v_mfma_f32_32x32x16_bf16 v[84:99], v[174:177], v[136:139], v[84:99]
	ds_read_b128 v[174:177], v205 offset:20064
	v_exp_f32_e32 v22, v22
	v_add_f32_e32 v179, v5, v179
	v_exp_f32_e32 v6, v6
	v_add_f32_e32 v179, v22, v179
	s_waitcnt lgkmcnt(4)
	v_mfma_f32_32x32x16_bf16 v[68:83], v[206:209], v[136:139], v[68:83]
	ds_read_b128 v[206:209], v205 offset:13440
	v_cvt_pk_bf16_f32 v108, v4, v5
	v_exp_f32_e32 v23, v23
	v_add_f32_e32 v179, v6, v179
	v_exp_f32_e32 v7, v7
	s_waitcnt lgkmcnt(4)
	v_mfma_f32_32x32x16_bf16 v[84:99], v[226:229], v[140:143], v[84:99]
	ds_read_b128 v[226:229], v205 offset:20096
	v_add_f32_e32 v179, v23, v179
	v_cvt_pk_bf16_f32 v101, v22, v23
	v_exp_f32_e32 v24, v24
	v_add_f32_e32 v179, v7, v179
	s_waitcnt lgkmcnt(4)
	v_mfma_f32_32x32x16_bf16 v[68:83], v[166:169], v[140:143], v[68:83]
	ds_read_b128 v[166:169], v205 offset:13472
	v_exp_f32_e32 v8, v8
	v_add_f32_e32 v179, v24, v179
	v_cvt_pk_bf16_f32 v109, v6, v7
	v_exp_f32_e32 v25, v25
	s_waitcnt lgkmcnt(4)
	v_mfma_f32_32x32x16_bf16 v[84:99], v[170:173], v[144:147], v[84:99]
	ds_read_b128 v[170:173], v205 offset:20128
	v_add_f32_e32 v179, v8, v179
	v_exp_f32_e32 v9, v9
	v_add_f32_e32 v179, v25, v179
	v_cvt_pk_bf16_f32 v102, v24, v25
	s_waitcnt lgkmcnt(4)
	v_mfma_f32_32x32x16_bf16 v[68:83], v[174:177], v[144:147], v[68:83]
	ds_read_b128 v[174:177], v178 offset:58368
	v_exp_f32_e32 v26, v26
	v_add_f32_e32 v179, v9, v179
	v_exp_f32_e32 v10, v10
	v_add_f32_e32 v179, v26, v179
	s_waitcnt lgkmcnt(4)
	v_mfma_f32_32x32x16_bf16 v[84:99], v[206:209], v[148:151], v[84:99]
	ds_read_b128 v[206:209], v178 offset:62976
	s_waitcnt vmcnt(0)
	ds_write_b128 v219, v[156:159] offset:0
	v_cvt_pk_bf16_f32 v110, v8, v9
	v_exp_f32_e32 v27, v27
	v_add_f32_e32 v179, v10, v179
	v_exp_f32_e32 v11, v11
	s_waitcnt lgkmcnt(5)
	v_mfma_f32_32x32x16_bf16 v[68:83], v[226:229], v[148:151], v[68:83]
	ds_read_b128 v[226:229], v178 offset:58400
	ds_write_b64 v220, v[160:161] offset:0
	v_add_f32_e32 v179, v27, v179
	v_cvt_pk_bf16_f32 v103, v26, v27
	v_exp_f32_e32 v28, v28
	v_add_f32_e32 v179, v11, v179
	s_waitcnt lgkmcnt(6)
	v_mfma_f32_32x32x16_bf16 v[84:99], v[166:169], v[152:155], v[84:99]
	ds_read_b128 v[166:169], v178 offset:63008
	ds_write_b64 v221, v[162:163] offset:35840
	v_exp_f32_e32 v29, v29
	v_add_f32_e32 v179, v28, v179
	v_cvt_pk_bf16_f32 v111, v10, v11
	v_exp_f32_e32 v30, v30
	s_waitcnt lgkmcnt(7)
	v_mfma_f32_32x32x16_bf16 v[68:83], v[170:173], v[152:155], v[68:83]
	ds_read_b128 v[170:173], v178 offset:58432
	ds_write_b64 v222, v[164:165] offset:35840
	v_add_f32_e32 v179, v29, v179
	v_exp_f32_e32 v31, v31
	v_add_f32_e32 v179, v30, v179
	v_cvt_pk_bf16_f32 v104, v28, v29
	s_waitcnt lgkmcnt(8)
	v_mfma_f32_32x32x16_bf16 v[36:51], v[174:177], v[116:119], v[36:51]
	ds_read_b128 v[174:177], v178 offset:63040
	v_lshl_add_u32 v156, s12, v215, v223
	global_load_dwordx4 v[156:159], v156, s[44:45]
	v_exp_f32_e32 v32, v32
	v_add_f32_e32 v179, v31, v179
	v_exp_f32_e32 v33, v33
	v_add_f32_e32 v179, v32, v179
	s_waitcnt lgkmcnt(8)
	v_mfma_f32_32x32x16_bf16 v[52:67], v[206:209], v[116:119], v[52:67]
	ds_read_b128 v[206:209], v178 offset:58464
	v_mad_u32_u24 v160, s12, v199, v202
	global_load_dwordx2 v[160:161], v160, s[44:45]
	s_add_i32 s12, s12, 1
	s_cmp_eq_u32 s12, s34
	s_cselect_b32 s12, 0, s12
	v_cvt_pk_bf16_f32 v105, v30, v31
	v_exp_f32_e32 v34, v34
	v_add_f32_e32 v179, v33, v179
	v_exp_f32_e32 v35, v35
	s_waitcnt lgkmcnt(7)
	v_mfma_f32_32x32x16_bf16 v[36:51], v[226:229], v[120:123], v[36:51]
	ds_read_b128 v[226:229], v178 offset:63072
	v_lshl_add_u32 v162, s13, 7, v204
	global_load_dwordx4 v[162:165], v162, s[44:45]
	s_add_i32 s13, s13, 1
	s_cmp_eq_u32 s13, s34
	s_cselect_b32 s13, 0, s13
	v_add_f32_e32 v179, v34, v179
	v_cvt_pk_bf16_f32 v106, v32, v33
	v_exp_f32_e32 v12, v12
	v_add_f32_e32 v179, v35, v179
	s_waitcnt lgkmcnt(6)
	v_mfma_f32_32x32x16_bf16 v[52:67], v[166:169], v[120:123], v[52:67]
	ds_read_b128 v[166:169], v205 offset:45056
	v_exp_f32_e32 v13, v13
	v_add_f32_e32 v179, v12, v179
	v_cvt_pk_bf16_f32 v107, v34, v35
	v_exp_f32_e32 v14, v14
	s_waitcnt lgkmcnt(5)
	v_mfma_f32_32x32x16_bf16 v[36:51], v[170:173], v[124:127], v[36:51]
	ds_read_b128 v[170:173], v205 offset:51712
	v_add_f32_e32 v179, v13, v179
	v_exp_f32_e32 v15, v15
	v_add_f32_e32 v179, v14, v179
	v_cvt_pk_bf16_f32 v112, v12, v13
	s_waitcnt lgkmcnt(4)
	v_mfma_f32_32x32x16_bf16 v[52:67], v[174:177], v[124:127], v[52:67]
	ds_read_b128 v[174:177], v205 offset:45088
	v_exp_f32_e32 v16, v16
	v_add_f32_e32 v179, v15, v179
	v_exp_f32_e32 v17, v17
	v_add_f32_e32 v179, v16, v179
	s_waitcnt lgkmcnt(4)
	v_mfma_f32_32x32x16_bf16 v[36:51], v[206:209], v[128:131], v[36:51]
	ds_read_b128 v[206:209], v205 offset:51744
	v_cvt_pk_bf16_f32 v113, v14, v15
	v_exp_f32_e32 v18, v18
	v_add_f32_e32 v179, v17, v179
	v_exp_f32_e32 v19, v19
	s_waitcnt lgkmcnt(4)
	v_mfma_f32_32x32x16_bf16 v[52:67], v[226:229], v[128:131], v[52:67]
	ds_read_b128 v[226:229], v205 offset:45120
	v_add_f32_e32 v179, v18, v179
	v_cvt_pk_bf16_f32 v114, v16, v17
	v_add_f32_e32 v179, v19, v179
	v_cvt_pk_bf16_f32 v115, v18, v19
	v_add_f32_e32 v224, v224, v179
	s_add_i32 s1, s1, 1
	s_barrier
	s_branch .Latt_u6_top
